# speedup vs baseline: 1.0586x; 1.0077x over previous
.LBB1_5:
	s_andn2_b64 vcc, exec, s[4:5]
	s_cbranch_vccnz .LBB1_41
	s_load_dwordx4 s[4:7], s[0:1], 0x0
	s_load_dwordx2 s[8:9], s[0:1], 0x40
	v_lshlrev_b32_e32 v2, 4, v0
	s_mov_b32 s29, 0
	v_mov_b32_e32 v3, 0
	s_lshl_b32 s28, s2, 4
	s_waitcnt lgkmcnt(0)
	v_lshl_add_u64 v[96:97], s[4:5], 0, v[2:3]
	s_lshl_b64 s[4:5], s[28:29], 12
	v_lshl_add_u64 v[4:5], v[96:97], 0, s[4:5]
	s_or_b32 s4, s28, 1
	s_mov_b32 s5, s29
	s_lshl_b64 s[10:11], s[4:5], 12
	s_or_b32 s20, s28, 2
	s_mov_b32 s21, s29
	v_lshl_add_u64 v[6:7], v[96:97], 0, s[10:11]
	global_load_dwordx4 v[30:33], v[4:5], off nt
	global_load_dwordx4 v[26:29], v[6:7], off nt
	s_lshl_b64 s[10:11], s[20:21], 12
	s_or_b32 s18, s28, 3
	s_mov_b32 s19, s29
	v_lshl_add_u64 v[4:5], v[96:97], 0, s[10:11]
	s_lshl_b64 s[10:11], s[18:19], 12
	global_load_dwordx4 v[22:25], v[4:5], off nt
	v_lshl_add_u64 v[4:5], v[96:97], 0, s[10:11]
	global_load_dwordx4 v[18:21], v[4:5], off nt
	s_or_b32 s16, s28, 4
	s_mov_b32 s17, s29
	s_lshl_b64 s[10:11], s[16:17], 12
	v_lshl_add_u64 v[4:5], v[96:97], 0, s[10:11]
	global_load_dwordx4 v[14:17], v[4:5], off nt
	s_or_b32 s14, s28, 5
	s_mov_b32 s15, s29
	s_lshl_b64 s[24:25], s[14:15], 12
	v_lshl_add_u64 v[42:43], s[6:7], 0, v[2:3]
	s_or_b32 s12, s28, 6
	s_mov_b32 s13, s29
	v_lshl_add_u64 v[4:5], v[96:97], 0, s[24:25]
	global_load_dwordx4 v[34:37], v2, s[6:7] nt
	v_lshlrev_b32_e32 v2, 3, v0
	v_add_co_u32_e32 v48, vcc, 0x1000, v42
	s_or_b32 s10, s28, 7
	s_mov_b32 s11, s29
	s_lshl_b64 s[26:27], s[12:13], 12
	global_load_dwordx4 v[10:13], v[4:5], off nt
	s_lshl_b64 s[4:5], s[4:5], 11
	v_lshl_add_u64 v[94:95], s[8:9], 0, v[2:3]
	s_mov_b64 s[6:7], vcc
	v_add_co_u32_e32 v46, vcc, 0x2000, v42
	s_lshl_b64 s[30:31], s[10:11], 12
	v_lshl_add_u64 v[38:39], v[96:97], 0, s[26:27]
	v_lshl_add_u64 v[52:53], v[94:95], 0, s[4:5]
	s_mov_b64 s[4:5], vcc
	v_add_co_u32_e32 v44, vcc, 0x3000, v42
	v_lshl_add_u64 v[40:41], v[96:97], 0, s[30:31]
	global_load_dwordx4 v[6:9], v[38:39], off nt
	global_load_dwordx4 v[2:5], v[40:41], off nt
	s_mov_b64 s[8:9], vcc
	v_add_co_u32_e32 v38, vcc, 0x4000, v42
	s_lshl_b64 s[22:23], s[28:29], 11
	s_nop 0
	v_addc_co_u32_e32 v39, vcc, 0, v43, vcc
	v_addc_co_u32_e64 v49, vcc, 0, v43, s[6:7]
	global_load_dwordx4 v[38:41], v[38:39], off nt
	v_lshl_add_u64 v[50:51], v[94:95], 0, s[22:23]
	global_load_dwordx4 v[54:57], v[48:49], off nt
	v_add_co_u32_e32 v48, vcc, 0x5000, v42
	s_lshl_b64 s[20:21], s[20:21], 11
	s_nop 0
	v_addc_co_u32_e32 v49, vcc, 0, v43, vcc
	global_load_dwordx4 v[58:61], v[48:49], off nt
	s_lshl_b64 s[6:7], s[18:19], 11
	s_movk_i32 s3, 0xc0
	s_waitcnt vmcnt(11)
	v_cvt_f16_f32_e32 v1, v30
	v_cvt_f16_f32_e32 v45, v33
	v_cvt_pk_f16_f32 v47, v31, v32
	s_waitcnt vmcnt(10)
	v_cvt_f16_f32_e32 v62, v26
	v_cvt_f16_f32_e32 v63, v29
	v_pack_b32_f16 v48, v1, v47
	v_alignbit_b32 v49, v45, v47, 16
	v_cvt_pk_f16_f32 v64, v27, v28
	v_pack_b32_f16 v62, v62, v64
	s_waitcnt vmcnt(8)
	v_cvt_f16_f32_e32 v1, v18
	v_cvt_f16_f32_e32 v47, v21
	v_cvt_pk_f16_f32 v45, v19, v20
	v_alignbit_b32 v63, v63, v64, 16
	global_store_dwordx2 v[50:51], v[48:49], off
	global_store_dwordx2 v[52:53], v[62:63], off
	v_pack_b32_f16 v50, v1, v45
	v_alignbit_b32 v51, v47, v45, 16
	s_waitcnt vmcnt(9)
	v_cvt_f16_f32_e32 v1, v14
	v_cvt_f16_f32_e32 v45, v17
	v_addc_co_u32_e64 v47, vcc, 0, v43, s[4:5]
	global_load_dwordx4 v[68:71], v[46:47], off nt
	v_add_co_u32_e32 v46, vcc, 0x6000, v42
	v_cvt_f16_f32_e32 v65, v22
	s_nop 0
	v_addc_co_u32_e32 v47, vcc, 0, v43, vcc
	global_load_dwordx4 v[86:89], v[46:47], off nt
	v_cvt_pk_f16_f32 v47, v15, v16
	v_pack_b32_f16 v46, v1, v47
	v_alignbit_b32 v47, v45, v47, 16
	v_addc_co_u32_e64 v45, vcc, 0, v43, s[8:9]
	global_load_dwordx4 v[98:101], v[44:45], off nt
	v_add_co_u32_e32 v42, vcc, 0x7000, v42
	v_cvt_f16_f32_e32 v67, v25
	s_nop 0
	v_addc_co_u32_e32 v43, vcc, 0, v43, vcc
	global_load_dwordx4 v[102:105], v[42:43], off nt
	v_cvt_pk_f16_f32 v66, v23, v24
	v_pack_b32_f16 v48, v65, v66
	v_alignbit_b32 v49, v67, v66, 16
	v_lshl_add_u64 v[52:53], v[94:95], 0, s[20:21]
	s_waitcnt vmcnt(11)
	v_cvt_f16_f32_e32 v1, v10
	global_store_dwordx2 v[52:53], v[48:49], off
	v_lshl_add_u64 v[48:49], v[94:95], 0, s[6:7]
	s_lshl_b64 s[4:5], s[16:17], 11
	global_store_dwordx2 v[48:49], v[50:51], off
	v_lshl_add_u64 v[48:49], v[94:95], 0, s[4:5]
	v_cvt_f16_f32_e32 v50, v13
	global_store_dwordx2 v[48:49], v[46:47], off
	v_cvt_pk_f16_f32 v47, v11, v12
	v_pack_b32_f16 v46, v1, v47
	s_waitcnt vmcnt(13)
	v_cvt_f16_f32_e32 v1, v6
	v_cvt_f16_f32_e32 v44, v9
	s_lshl_b64 s[4:5], s[14:15], 11
	v_alignbit_b32 v47, v50, v47, 16
	v_lshl_add_u64 v[42:43], v[94:95], 0, s[4:5]
	global_store_dwordx2 v[42:43], v[46:47], off
	v_cvt_pk_f16_f32 v42, v7, v8
	v_pack_b32_f16 v108, v1, v42
	v_alignbit_b32 v109, v44, v42, 16
	v_cvt_f64_f32_e32 v[52:53], v35
	s_waitcnt vmcnt(12)
	v_cvt_f64_f32_e32 v[42:43], v39
	v_cvt_f64_f32_e32 v[110:111], v31
	v_cvt_f64_f32_e32 v[48:49], v34
	v_cvt_f64_f32_e32 v[50:51], v36
	v_cvt_f64_f32_e32 v[46:47], v37
	v_cvt_f64_f32_e32 v[36:37], v38
	v_cvt_f64_f32_e32 v[106:107], v30
	v_cvt_f64_f32_e32 v[112:113], v32
	v_cvt_f64_f32_e32 v[114:115], v33
	v_mul_f64 v[30:31], v[52:53], v[110:111]
	v_mul_f64 v[32:33], v[42:43], v[110:111]
	v_cvt_f64_f32_e32 v[38:39], v40
	v_fmac_f64_e32 v[30:31], v[48:49], v[106:107]
	v_fmac_f64_e32 v[32:33], v[36:37], v[106:107]
	v_cvt_f64_f32_e32 v[34:35], v41
	v_fmac_f64_e32 v[30:31], v[50:51], v[112:113]
	v_fmac_f64_e32 v[32:33], v[38:39], v[112:113]
	v_and_b32_e32 v1, 1, v0
	v_fmac_f64_e32 v[30:31], v[46:47], v[114:115]
	v_fmac_f64_e32 v[32:33], v[34:35], v[114:115]
	v_cmp_eq_u32_e32 vcc, 0, v1
	s_waitcnt vmcnt(11)
	v_cvt_f64_f32_e32 v[74:75], v55
	s_waitcnt vmcnt(10)
	v_cvt_f64_f32_e32 v[44:45], v59
	v_cndmask_b32_e32 v1, v31, v33, vcc
	v_cndmask_b32_e32 v117, v33, v31, vcc
	v_cndmask_b32_e32 v116, v32, v30, vcc
	v_cndmask_b32_e32 v122, v30, v32, vcc
	v_cvt_f64_f32_e32 v[64:65], v54
	v_cvt_f64_f32_e32 v[66:67], v56
	v_cvt_f64_f32_e32 v[62:63], v57
	v_cvt_f64_f32_e32 v[32:33], v58
	v_mul_f64 v[54:55], v[74:75], v[110:111]
	v_mul_f64 v[56:57], v[44:45], v[110:111]
	v_cvt_f64_f32_e32 v[40:41], v60
	v_fmac_f64_e32 v[54:55], v[64:65], v[106:107]
	v_fmac_f64_e32 v[56:57], v[32:33], v[106:107]
	v_cvt_f64_f32_e32 v[30:31], v61
	v_fmac_f64_e32 v[54:55], v[66:67], v[112:113]
	v_fmac_f64_e32 v[56:57], v[40:41], v[112:113]
	v_fmac_f64_e32 v[54:55], v[62:63], v[114:115]
	v_fmac_f64_e32 v[56:57], v[30:31], v[114:115]
	s_waitcnt vmcnt(7)
	v_cvt_f64_f32_e32 v[84:85], v69
	v_cndmask_b32_e32 v119, v57, v55, vcc
	s_waitcnt vmcnt(6)
	v_cvt_f64_f32_e32 v[60:61], v87
	v_cndmask_b32_e32 v118, v56, v54, vcc
	v_cndmask_b32_e32 v123, v55, v57, vcc
	v_cndmask_b32_e32 v124, v54, v56, vcc
	v_cvt_f64_f32_e32 v[80:81], v68
	v_cvt_f64_f32_e32 v[82:83], v70
	s_waitcnt vmcnt(5)
	v_cvt_f64_f32_e32 v[90:91], v100
	v_mbcnt_lo_u32_b32 v100, -1, 0
	v_mbcnt_hi_u32_b32 v100, -1, v100
	v_cvt_f64_f32_e32 v[78:79], v71
	v_cvt_f64_f32_e32 v[56:57], v86
	v_mul_f64 v[68:69], v[84:85], v[110:111]
	v_mul_f64 v[70:71], v[60:61], v[110:111]
	v_cvt_f64_f32_e32 v[86:87], v101
	v_and_b32_e32 v101, 64, v100
	v_cvt_f64_f32_e32 v[58:59], v88
	v_fmac_f64_e32 v[68:69], v[80:81], v[106:107]
	v_fmac_f64_e32 v[70:71], v[56:57], v[106:107]
	v_add_u32_e32 v127, 64, v101
	v_xor_b32_e32 v101, 1, v100
	v_cvt_f64_f32_e32 v[54:55], v89
	v_fmac_f64_e32 v[68:69], v[82:83], v[112:113]
	v_fmac_f64_e32 v[70:71], v[58:59], v[112:113]
	v_cmp_lt_i32_e64 s[4:5], v101, v127
	v_fmac_f64_e32 v[68:69], v[78:79], v[114:115]
	v_fmac_f64_e32 v[70:71], v[54:55], v[114:115]
	v_cndmask_b32_e64 v101, v100, v101, s[4:5]
	v_cndmask_b32_e32 v125, v69, v71, vcc
	v_cndmask_b32_e32 v126, v68, v70, vcc
	v_cvt_f64_f32_e32 v[92:93], v99
	s_waitcnt vmcnt(4)
	v_cvt_f64_f32_e32 v[76:77], v103
	v_lshlrev_b32_e32 v101, 2, v101
	v_cndmask_b32_e32 v121, v71, v69, vcc
	v_cndmask_b32_e32 v120, v70, v68, vcc
	v_cvt_f64_f32_e32 v[88:89], v98
	v_cvt_f64_f32_e32 v[70:71], v102
	v_mul_f64 v[98:99], v[92:93], v[110:111]
	v_mul_f64 v[102:103], v[76:77], v[110:111]
	ds_bpermute_b32 v110, v101, v126
	ds_bpermute_b32 v111, v101, v125
	v_cvt_f64_f32_e32 v[72:73], v104
	v_fmac_f64_e32 v[98:99], v[88:89], v[106:107]
	v_fmac_f64_e32 v[102:103], v[70:71], v[106:107]
	v_cvt_f64_f32_e32 v[68:69], v105
	v_fmac_f64_e32 v[98:99], v[90:91], v[112:113]
	v_fmac_f64_e32 v[102:103], v[72:73], v[112:113]
	ds_bpermute_b32 v106, v101, v122
	ds_bpermute_b32 v107, v101, v1
	v_fmac_f64_e32 v[98:99], v[86:87], v[114:115]
	v_fmac_f64_e32 v[102:103], v[68:69], v[114:115]
	v_cndmask_b32_e32 v1, v99, v103, vcc
	v_cndmask_b32_e32 v112, v98, v102, vcc
	v_cndmask_b32_e32 v105, v103, v99, vcc
	v_cndmask_b32_e32 v104, v102, v98, vcc
	s_waitcnt lgkmcnt(2)
	v_add_f64 v[102:103], v[120:121], v[110:111]
	ds_bpermute_b32 v110, v101, v112
	ds_bpermute_b32 v111, v101, v1
	s_waitcnt lgkmcnt(2)
	v_add_f64 v[98:99], v[116:117], v[106:107]
	ds_bpermute_b32 v106, v101, v124
	ds_bpermute_b32 v107, v101, v123
	v_and_b32_e32 v113, 2, v0
	s_waitcnt lgkmcnt(2)
	v_add_f64 v[110:111], v[104:105], v[110:111]
	v_xor_b32_e32 v104, 2, v100
	v_cmp_lt_i32_e64 s[4:5], v104, v127
	v_cmp_eq_u32_e64 s[8:9], 0, v113
	s_waitcnt lgkmcnt(0)
	v_add_f64 v[106:107], v[118:119], v[106:107]
	v_cndmask_b32_e64 v104, v100, v104, s[4:5]
	v_cndmask_b32_e64 v113, v103, v99, s[8:9]
	v_cndmask_b32_e64 v1, v99, v103, s[8:9]
	v_cndmask_b32_e64 v99, v98, v102, s[8:9]
	v_cndmask_b32_e64 v103, v107, v111, s[8:9]
	v_cndmask_b32_e64 v105, v106, v110, s[8:9]
	v_lshlrev_b32_e32 v104, 2, v104
	ds_bpermute_b32 v114, v104, v99
	ds_bpermute_b32 v115, v104, v1
	ds_bpermute_b32 v116, v104, v105
	ds_bpermute_b32 v117, v104, v103
	v_cndmask_b32_e64 v112, v102, v98, s[8:9]
	v_cndmask_b32_e64 v99, v111, v107, s[8:9]
	v_cndmask_b32_e64 v98, v110, v106, s[8:9]
	v_and_b32_e32 v1, 4, v0
	s_waitcnt lgkmcnt(2)
	v_add_f64 v[102:103], v[112:113], v[114:115]
	s_waitcnt lgkmcnt(0)
	v_add_f64 v[98:99], v[98:99], v[116:117]
	v_cmp_eq_u32_e64 s[4:5], 0, v1
	s_nop 1
	v_cndmask_b32_e64 v107, v99, v103, s[4:5]
	v_cndmask_b32_e64 v1, v103, v99, s[4:5]
	v_xor_b32_e32 v103, 4, v100
	v_cmp_lt_i32_e64 s[6:7], v103, v127
	v_cndmask_b32_e64 v99, v102, v98, s[4:5]
	v_cndmask_b32_e64 v106, v98, v102, s[4:5]
	v_cndmask_b32_e64 v103, v100, v103, s[6:7]
	v_lshlrev_b32_e32 v105, 2, v103
	ds_bpermute_b32 v110, v105, v99
	ds_bpermute_b32 v111, v105, v1
	s_lshl_b64 s[6:7], s[12:13], 11
	v_xor_b32_e32 v102, 8, v100
	v_lshl_add_u64 v[112:113], v[94:95], 0, s[6:7]
	v_cmp_lt_i32_e64 s[6:7], v102, v127
	v_cvt_f16_f32_e32 v1, v2
	s_waitcnt lgkmcnt(0)
	v_add_f64 v[98:99], v[106:107], v[110:111]
	v_cndmask_b32_e64 v102, v100, v102, s[6:7]
	v_lshlrev_b32_e32 v106, 2, v102
	ds_bpermute_b32 v102, v106, v98
	ds_bpermute_b32 v103, v106, v99
	v_cvt_pk_f16_f32 v110, v3, v4
	global_store_dwordx2 v[112:113], v[108:109], off
	v_pack_b32_f16 v108, v1, v110
	v_xor_b32_e32 v1, 16, v100
	v_cmp_lt_i32_e64 s[6:7], v1, v127
	v_cvt_f16_f32_e32 v109, v5
	s_waitcnt lgkmcnt(0)
	v_add_f64 v[98:99], v[98:99], v[102:103]
	v_cndmask_b32_e64 v1, v100, v1, s[6:7]
	v_lshlrev_b32_e32 v107, 2, v1
	ds_bpermute_b32 v102, v107, v98
	ds_bpermute_b32 v103, v107, v99
	s_lshl_b64 s[6:7], s[10:11], 11
	v_xor_b32_e32 v1, 32, v100
	v_alignbit_b32 v109, v109, v110, 16
	v_lshl_add_u64 v[110:111], v[94:95], 0, s[6:7]
	v_cmp_lt_i32_e64 s[6:7], v1, v127
	global_store_dwordx2 v[110:111], v[108:109], off
	s_waitcnt lgkmcnt(0)
	v_add_f64 v[98:99], v[98:99], v[102:103]
	v_cndmask_b32_e64 v1, v100, v1, s[6:7]
	v_lshlrev_b32_e32 v109, 2, v1
	ds_bpermute_b32 v102, v109, v98
	ds_bpermute_b32 v103, v109, v99
	v_bfrev_b32_e32 v1, v0
	v_lshrrev_b32_e32 v1, 26, v1
	v_and_b32_e32 v100, 56, v0
	v_and_b32_e32 v1, 56, v1
	v_cmp_eq_u32_e64 s[6:7], 0, v100
	v_and_or_b32 v108, v0, s3, v1
	v_mov_b32_e32 v100, v27
	v_mov_b32_e32 v27, v28
	v_mov_b32_e32 v28, v23
	v_mov_b32_e32 v23, v24
	v_mov_b32_e32 v24, v19
	v_mov_b32_e32 v19, v20
	v_mov_b32_e32 v20, v15
	v_mov_b32_e32 v15, v16
	v_mov_b32_e32 v16, v11
	v_mov_b32_e32 v11, v12
	v_mov_b32_e32 v12, v7
	v_mov_b32_e32 v7, v8
	v_mov_b32_e32 v8, v3
	v_mov_b32_e32 v1, v4
	s_and_saveexec_b64 s[10:11], s[6:7]
	s_cbranch_execz .LBB1_8
	s_waitcnt lgkmcnt(0)
	v_add_f64 v[98:99], v[98:99], v[102:103]
	ds_write_b64 v108, v[98:99]

.LBB1_22:
	s_or_b64 exec, exec, s[10:11]
	s_or_b32 s14, s28, 8
	s_mov_b32 s15, 0
	s_lshl_b64 s[10:11], s[14:15], 12
	v_lshl_add_u64 v[2:3], v[96:97], 0, s[10:11]
	global_load_dwordx4 v[110:113], v[2:3], off nt
	s_or_b32 s16, s28, 9
	s_mov_b32 s17, s15
	s_lshl_b64 s[10:11], s[16:17], 12
	v_lshl_add_u64 v[2:3], v[96:97], 0, s[10:11]
	global_load_dwordx4 v[26:29], v[2:3], off nt
	s_or_b32 s18, s28, 10
	s_mov_b32 s19, s15
	s_lshl_b64 s[10:11], s[18:19], 12
	s_or_b32 s20, s28, 11
	s_mov_b32 s21, s15
	v_lshl_add_u64 v[2:3], v[96:97], 0, s[10:11]
	s_lshl_b64 s[10:11], s[20:21], 12
	global_load_dwordx4 v[22:25], v[2:3], off nt
	v_lshl_add_u64 v[2:3], v[96:97], 0, s[10:11]
	global_load_dwordx4 v[18:21], v[2:3], off nt
	s_or_b32 s22, s28, 12
	s_mov_b32 s23, s15
	s_lshl_b64 s[10:11], s[22:23], 12
	s_or_b32 s24, s28, 13
	s_mov_b32 s25, s15
	v_lshl_add_u64 v[2:3], v[96:97], 0, s[10:11]
	s_lshl_b64 s[10:11], s[24:25], 12
	global_load_dwordx4 v[14:17], v[2:3], off nt
	v_lshl_add_u64 v[2:3], v[96:97], 0, s[10:11]
	global_load_dwordx4 v[10:13], v[2:3], off nt
	s_or_b32 s12, s28, 14
	s_mov_b32 s13, s15
	s_lshl_b64 s[10:11], s[12:13], 12
	v_lshl_add_u64 v[2:3], v[96:97], 0, s[10:11]
	global_load_dwordx4 v[6:9], v[2:3], off nt
	s_or_b32 s10, s28, 15
	s_mov_b32 s11, s15
	s_lshl_b64 s[26:27], s[10:11], 12
	v_lshl_add_u64 v[2:3], v[96:97], 0, s[26:27]
	s_waitcnt lgkmcnt(0)
	global_load_dwordx4 v[2:5], v[2:3], off nt
	s_lshl_b64 s[14:15], s[14:15], 11
	v_lshl_add_u64 v[98:99], v[94:95], 0, s[14:15]
	s_lshl_b64 s[14:15], s[16:17], 11
	v_lshl_add_u64 v[102:103], v[94:95], 0, s[14:15]
	s_lshl_b64 s[16:17], s[18:19], 11
	s_lshl_b64 s[18:19], s[20:21], 11
	s_lshl_b64 s[20:21], s[22:23], 11
	s_lshl_b64 s[22:23], s[24:25], 11
	v_lshl_add_u64 v[114:115], v[94:95], 0, s[16:17]
	s_lshl_b64 s[12:13], s[12:13], 11
	v_lshl_add_u64 v[116:117], v[94:95], 0, s[18:19]
	v_lshl_add_u64 v[118:119], v[94:95], 0, s[20:21]
	v_lshl_add_u64 v[120:121], v[94:95], 0, s[22:23]
	s_lshl_b64 s[10:11], s[10:11], 11
	s_waitcnt vmcnt(7)
	v_cvt_f16_f32_e32 v1, v110
	v_cvt_pk_f16_f32 v97, v111, v112
	v_cvt_f16_f32_e32 v100, v113
	v_pack_b32_f16 v122, v1, v97
	s_waitcnt vmcnt(6)
	v_cvt_f16_f32_e32 v124, v26
	v_cvt_f16_f32_e32 v1, v29
	v_mov_b32_e32 v96, v27
	v_cvt_pk_f16_f32 v27, v27, v28
	v_alignbit_b32 v123, v100, v97, 16
	global_store_dwordx2 v[98:99], v[122:123], off
	v_pack_b32_f16 v98, v124, v27
	v_alignbit_b32 v99, v1, v27, 16
	s_waitcnt vmcnt(6)
	v_cvt_f16_f32_e32 v97, v22
	v_cvt_pk_f16_f32 v100, v23, v24
	s_waitcnt vmcnt(5)
	v_cvt_f16_f32_e32 v123, v18
	v_cvt_f16_f32_e32 v27, v21
	v_cvt_pk_f16_f32 v1, v19, v20
	v_cvt_f16_f32_e32 v122, v25
	global_store_dwordx2 v[102:103], v[98:99], off
	v_pack_b32_f16 v98, v97, v100
	v_pack_b32_f16 v102, v123, v1
	v_alignbit_b32 v103, v27, v1, 16
	s_waitcnt vmcnt(5)
	v_cvt_f16_f32_e32 v124, v14
	v_cvt_f16_f32_e32 v126, v17
	s_waitcnt vmcnt(4)
	v_cvt_f16_f32_e32 v97, v10
	v_cvt_f16_f32_e32 v1, v13
	v_cvt_pk_f16_f32 v125, v15, v16
	v_cvt_pk_f16_f32 v27, v11, v12
	v_alignbit_b32 v99, v122, v100, 16
	v_pack_b32_f16 v122, v124, v125
	v_alignbit_b32 v123, v126, v125, 16
	v_pack_b32_f16 v124, v97, v27
	v_alignbit_b32 v125, v1, v27, 16
	s_waitcnt vmcnt(3)
	v_cvt_f16_f32_e32 v1, v6
	v_cvt_f16_f32_e32 v27, v9
	v_cvt_pk_f16_f32 v97, v7, v8
	global_store_dwordx2 v[114:115], v[98:99], off
	global_store_dwordx2 v[116:117], v[102:103], off
	global_store_dwordx2 v[118:119], v[122:123], off
	global_store_dwordx2 v[120:121], v[124:125], off
	v_pack_b32_f16 v98, v1, v97
	v_alignbit_b32 v99, v27, v97, 16
	v_lshl_add_u64 v[102:103], v[94:95], 0, s[12:13]
	global_store_dwordx2 v[102:103], v[98:99], off
	v_cvt_f64_f32_e32 v[102:103], v111
	v_cvt_f64_f32_e32 v[98:99], v110
	v_mul_f64 v[114:115], v[52:53], v[102:103]
	v_mul_f64 v[122:123], v[42:43], v[102:103]
	v_cvt_f64_f32_e32 v[110:111], v112
	v_fmac_f64_e32 v[114:115], v[48:49], v[98:99]
	v_fmac_f64_e32 v[122:123], v[36:37], v[98:99]
	v_cvt_f64_f32_e32 v[112:113], v113
	v_fmac_f64_e32 v[114:115], v[50:51], v[110:111]
	v_fmac_f64_e32 v[122:123], v[38:39], v[110:111]
	v_mul_f64 v[116:117], v[74:75], v[102:103]
	v_mul_f64 v[118:119], v[84:85], v[102:103]
	v_mul_f64 v[120:121], v[92:93], v[102:103]
	v_mul_f64 v[124:125], v[44:45], v[102:103]
	v_mul_f64 v[126:127], v[60:61], v[102:103]
	v_mul_f64 v[102:103], v[76:77], v[102:103]
	v_fmac_f64_e32 v[114:115], v[46:47], v[112:113]
	v_fmac_f64_e32 v[122:123], v[34:35], v[112:113]
	v_fmac_f64_e32 v[116:117], v[64:65], v[98:99]
	v_fmac_f64_e32 v[118:119], v[80:81], v[98:99]
	v_fmac_f64_e32 v[120:121], v[88:89], v[98:99]
	v_fmac_f64_e32 v[124:125], v[32:33], v[98:99]
	v_fmac_f64_e32 v[126:127], v[56:57], v[98:99]
	v_fmac_f64_e32 v[102:103], v[70:71], v[98:99]
	v_mov_b32_e32 v27, v28
	v_cndmask_b32_e32 v1, v115, v123, vcc
	v_cndmask_b32_e32 v28, v114, v122, vcc
	v_fmac_f64_e32 v[116:117], v[66:67], v[110:111]
	v_fmac_f64_e32 v[118:119], v[82:83], v[110:111]
	v_fmac_f64_e32 v[120:121], v[90:91], v[110:111]
	v_fmac_f64_e32 v[124:125], v[40:41], v[110:111]
	v_fmac_f64_e32 v[126:127], v[58:59], v[110:111]
	v_fmac_f64_e32 v[102:103], v[72:73], v[110:111]
	ds_bpermute_b32 v110, v101, v28
	ds_bpermute_b32 v111, v101, v1
	v_fmac_f64_e32 v[116:117], v[62:63], v[112:113]
	v_fmac_f64_e32 v[118:119], v[78:79], v[112:113]
	v_fmac_f64_e32 v[124:125], v[30:31], v[112:113]
	v_fmac_f64_e32 v[126:127], v[54:55], v[112:113]
	v_fmac_f64_e32 v[120:121], v[86:87], v[112:113]
	v_fmac_f64_e32 v[102:103], v[68:69], v[112:113]
	v_cndmask_b32_e32 v99, v123, v115, vcc
	v_cndmask_b32_e32 v98, v122, v114, vcc
	v_cndmask_b32_e32 v1, v117, v125, vcc
	v_cndmask_b32_e32 v97, v116, v124, vcc
	v_cndmask_b32_e32 v112, v124, v116, vcc
	v_cndmask_b32_e32 v100, v119, v127, vcc
	v_cndmask_b32_e32 v116, v118, v126, vcc
	v_cndmask_b32_e32 v113, v125, v117, vcc
	v_cndmask_b32_e32 v115, v127, v119, vcc
	v_cndmask_b32_e32 v114, v126, v118, vcc
	v_cndmask_b32_e32 v119, v121, v103, vcc
	v_cndmask_b32_e32 v118, v120, v102, vcc
	s_waitcnt lgkmcnt(0)
	v_add_f64 v[98:99], v[98:99], v[110:111]
	ds_bpermute_b32 v110, v101, v97
	ds_bpermute_b32 v111, v101, v1
	ds_bpermute_b32 v116, v101, v116
	ds_bpermute_b32 v117, v101, v100
	ds_bpermute_b32 v118, v101, v118
	ds_bpermute_b32 v119, v101, v119
	v_cndmask_b32_e32 v103, v103, v121, vcc
	v_cndmask_b32_e32 v102, v102, v120, vcc
	s_waitcnt lgkmcnt(4)
	v_add_f64 v[110:111], v[112:113], v[110:111]
	s_waitcnt lgkmcnt(2)
	v_add_f64 v[112:113], v[114:115], v[116:117]
	v_mov_b32_e32 v28, v23
	v_mov_b32_e32 v23, v24
	v_mov_b32_e32 v24, v19
	v_mov_b32_e32 v19, v20
	s_waitcnt lgkmcnt(0)
	v_add_f64 v[102:103], v[102:103], v[118:119]
	v_cndmask_b32_e64 v1, v99, v113, s[8:9]
	v_cndmask_b32_e64 v20, v98, v112, s[8:9]
	v_cndmask_b32_e64 v99, v113, v99, s[8:9]
	v_cndmask_b32_e64 v98, v112, v98, s[8:9]
	ds_bpermute_b32 v112, v104, v20
	ds_bpermute_b32 v113, v104, v1
	v_cndmask_b32_e64 v1, v111, v103, s[8:9]
	v_cndmask_b32_e64 v20, v110, v102, s[8:9]
	ds_bpermute_b32 v114, v104, v20
	ds_bpermute_b32 v115, v104, v1
	v_cndmask_b32_e64 v103, v103, v111, s[8:9]
	v_cndmask_b32_e64 v102, v102, v110, s[8:9]
	s_waitcnt lgkmcnt(2)
	v_add_f64 v[98:99], v[98:99], v[112:113]
	v_mov_b32_e32 v20, v15
	s_waitcnt lgkmcnt(0)
	v_add_f64 v[102:103], v[102:103], v[114:115]
	v_mov_b32_e32 v15, v16
	v_cndmask_b32_e64 v1, v99, v103, s[4:5]
	v_cndmask_b32_e64 v16, v98, v102, s[4:5]
	ds_bpermute_b32 v110, v105, v16
	ds_bpermute_b32 v111, v105, v1
	v_cndmask_b32_e64 v99, v103, v99, s[4:5]
	v_cndmask_b32_e64 v98, v102, v98, s[4:5]
	s_waitcnt vmcnt(7)
	v_cvt_f16_f32_e32 v1, v2
	v_cvt_f16_f32_e32 v16, v5
	s_waitcnt lgkmcnt(0)
	v_add_f64 v[98:99], v[98:99], v[110:111]
	ds_bpermute_b32 v102, v106, v98
	ds_bpermute_b32 v103, v106, v99
	v_cvt_pk_f16_f32 v97, v3, v4
	v_pack_b32_f16 v110, v1, v97
	v_alignbit_b32 v111, v16, v97, 16
	v_lshl_add_u64 v[94:95], v[94:95], 0, s[10:11]
	s_waitcnt lgkmcnt(0)
	v_add_f64 v[98:99], v[98:99], v[102:103]
	ds_bpermute_b32 v102, v107, v98
	ds_bpermute_b32 v103, v107, v99
	global_store_dwordx2 v[94:95], v[110:111], off
	v_mov_b32_e32 v16, v11
	v_mov_b32_e32 v11, v12
	v_mov_b32_e32 v12, v7
	s_waitcnt lgkmcnt(0)
	v_add_f64 v[94:95], v[98:99], v[102:103]
	ds_bpermute_b32 v98, v109, v94
	ds_bpermute_b32 v99, v109, v95
	v_mov_b32_e32 v7, v8
	v_mov_b32_e32 v8, v3
	v_mov_b32_e32 v1, v4
	s_and_saveexec_b64 s[10:11], s[6:7]
	s_cbranch_execz .LBB1_24
	s_waitcnt lgkmcnt(0)
	v_add_f64 v[94:95], v[94:95], v[98:99]
	ds_write_b64 v108, v[94:95] offset:2048
